# L1/L2: per-wave A tile stride 160 B (conflict-free ds_read_b128), moved into the old W region
# speedup vs baseline: 1.0163x; 1.0075x over previous
.LBB4_14:
	v_lshrrev_b32_e32 v2, 3, v0
	s_load_dwordx2 s[4:5], s[0:1], 0x40
	v_and_b32_e32 v2, 0x78, v2
	s_movk_i32 s2, 0xa0
	v_and_b32_e32 v97, 7, v0
	s_sub_i32 s0, s18, s8
	v_and_b32_e32 v1, 63, v0
	v_mov_b32_e32 v89, 0
	v_mad_u32_u24 v3, v2, s2, 0
	v_bfe_u32 v96, v0, 3, 3
	v_and_b32_e32 v99, 15, v0
	v_bfe_u32 v4, v0, 4, 2
	s_add_i32 s0, s0, 7
	v_mul_u32_u24_e32 v5, 0xa0, v97
	v_and_b32_e32 v0, 48, v0
	s_ashr_i32 s9, s0, 3
	v_cmp_eq_u32_e64 s[0:1], 0, v1
	v_mad_u32_u24 v1, v96, s2, v3
	v_lshlrev_b32_e32 v2, 3, v4
	v_add3_u32 v103, v3, v5, v0
	v_mov_b32_e32 v3, v89
	v_lshlrev_b32_e32 v98, 4, v97
	v_add_u32_e32 v0, 0, v0
	v_lshlrev_b32_e32 v88, 2, v4
	v_lshl_add_u64 v[90:91], s[22:23], 0, v[2:3]
	v_mul_u32_u24_e32 v2, 0x220, v99
	v_or_b32_e32 v100, 8, v97
	v_or_b32_e32 v101, 16, v97
	v_add_u32_e32 v102, 0, v98
	v_cmp_gt_u32_e64 s[2:3], 8, v99
	s_waitcnt lgkmcnt(0)
	v_lshl_add_u64 v[92:93], s[4:5], 0, v[88:89]
	v_lshlrev_b32_e32 v88, 2, v88
	v_add_u32_e32 v104, v1, v98
	v_add_u32_e32 v105, v0, v2
	v_add_u32_e32 v105, 0x1cd90, v105
	s_lshl_b32 s19, s36, 3
	s_add_i32 s19, s19, s8
	v_add_u32_e32 v94, s19, v96
	v_cmp_gt_i32_e64 s[4:5], s18, v94
	v_mov_b32_e32 v32, 0
	v_mov_b32_e32 v33, 0
	v_mov_b32_e32 v34, 0
	v_mov_b32_e32 v35, 0
	s_and_saveexec_b64 s[6:7], s[4:5]
	v_lshl_add_u32 v36, v94, 1, v94
	v_lshlrev_b32_e32 v36, 2, v36
	global_load_dwordx4 v[32:35], v36, s[10:11]
	s_mov_b64 exec, s[6:7]
	s_waitcnt vmcnt(6)
	ds_write_b128 v40, v[6:9]
	s_waitcnt vmcnt(5)
	ds_write_b128 v40, v[10:13] offset:17408
	s_waitcnt vmcnt(4)
	ds_write_b128 v41, v[14:17]
	s_waitcnt vmcnt(3)
	ds_write_b128 v41, v[18:21] offset:16384
	s_waitcnt vmcnt(2)
	ds_write_b128 v41, v[22:25] offset:32768
	s_waitcnt vmcnt(1)
	ds_write_b128 v41, v[26:29] offset:49152
	s_and_saveexec_b64 s[6:7], s[34:35]
	ds_write_b128 v38, v[42:45]
	s_mov_b64 exec, s[6:7]
	s_waitcnt vmcnt(0)
	v_sub_u32_e32 v72, v33, v32
	v_sub_u32_e32 v108, v34, v33
	v_sub_u32_e32 v35, v35, v34
	v_add_lshl_u32 v37, v32, v97, 2
	v_add_lshl_u32 v38, v33, v97, 2
	v_add_lshl_u32 v39, v34, v97, 2
	v_mov_b32_e32 v36, 0x4000000
	v_mov_b32_e32 v68, 0x4000000
	v_mov_b32_e32 v74, 0x4000000
	v_mov_b32_e32 v85, 0x4000000
	v_mov_b32_e32 v84, 0x4000000
	v_mov_b32_e32 v109, 0x4000000
	v_mov_b32_e32 v107, 0x4000000
	v_mov_b32_e32 v106, 0x4000000
	v_mov_b32_e32 v95, 0x4000000
	s_mov_b64 s[6:7], exec
	v_cmp_lt_i32_e32 vcc, v97, v72
	s_and_b64 exec, exec, vcc
	global_load_dword v36, v37, s[12:13]
	v_cmp_lt_i32_e32 vcc, v100, v72
	s_and_b64 exec, exec, vcc
	global_load_dword v68, v37, s[12:13] offset:32
	v_cmp_lt_i32_e32 vcc, v101, v72
	s_and_b64 exec, exec, vcc
	global_load_dword v74, v37, s[12:13] offset:64
	s_mov_b64 exec, s[6:7]
	v_cmp_lt_i32_e32 vcc, v97, v108
	s_and_b64 exec, exec, vcc
	global_load_dword v85, v38, s[12:13]
	v_cmp_lt_i32_e32 vcc, v100, v108
	s_and_b64 exec, exec, vcc
	global_load_dword v84, v38, s[12:13] offset:32
	v_cmp_lt_i32_e32 vcc, v101, v108
	s_and_b64 exec, exec, vcc
	global_load_dword v109, v38, s[12:13] offset:64
	s_mov_b64 exec, s[6:7]
	v_cmp_lt_i32_e32 vcc, v97, v35
	s_and_b64 exec, exec, vcc
	global_load_dword v107, v39, s[12:13]
	v_cmp_lt_i32_e32 vcc, v100, v35
	s_and_b64 exec, exec, vcc
	global_load_dword v106, v39, s[12:13] offset:32
	v_cmp_lt_i32_e32 vcc, v101, v35
	s_and_b64 exec, exec, vcc
	global_load_dword v95, v39, s[12:13] offset:64
	s_mov_b64 exec, s[6:7]
	s_waitcnt lgkmcnt(0)
	s_barrier
	s_cmp_ge_i32 s36, s9
	s_cbranch_scc1 .LBB4_103
	s_branch .Lp1_after_idx

.LBB4_61:
	ds_write_b128 v104, v[52:55]
	ds_read_b128 v[36:39], v105
	ds_read_b128 v[40:43], v103
	ds_read_b128 v[44:47], v105 offset:8704
	ds_read_b128 v[48:51], v105 offset:17408
	ds_read_b128 v[52:55], v105 offset:26112
	s_waitcnt lgkmcnt(3)
	v_mfma_f32_16x16x32_f16 v[36:39], v[36:39], v[40:43], 0
	s_waitcnt lgkmcnt(2)
	v_mfma_f32_16x16x32_f16 v[44:47], v[44:47], v[40:43], 0
	s_waitcnt lgkmcnt(1)
	v_mfma_f32_16x16x32_f16 v[48:51], v[48:51], v[40:43], 0
	s_waitcnt lgkmcnt(0)
	v_mfma_f32_16x16x32_f16 v[52:55], v[52:55], v[40:43], 0
	ds_read_b128 v[40:43], v105 offset:64
	ds_read_b128 v[56:59], v103 offset:64
	ds_read_b128 v[60:63], v105 offset:8768
	ds_read_b128 v[64:67], v105 offset:17472
	s_waitcnt lgkmcnt(2)
	v_mfma_f32_16x16x32_f16 v[36:39], v[40:43], v[56:59], v[36:39]
	v_cmp_lt_i32_e32 vcc, 8, v108
	s_cmp_lg_u64 vcc, 0
	v_add_u32_dpp v32, v85, v102 row_newbcast:0 row_mask:0xf bank_mask:0x3
	v_add_u32_dpp v32, v85, v102 row_newbcast:8 row_mask:0xf bank_mask:0xc
	s_waitcnt lgkmcnt(1)
	v_mfma_f32_16x16x32_f16 v[40:43], v[60:63], v[56:59], v[44:47]
	ds_read_b128 v[60:63], v105 offset:26176
	ds_read_b128 v[68:71], v32 offset:52240
	s_waitcnt lgkmcnt(2)
	v_mfma_f32_16x16x32_f16 v[44:47], v[64:67], v[56:59], v[48:51]
	v_add_u32_dpp v64, v85, v102 row_newbcast:1 row_mask:0xf bank_mask:0x3
	v_add_u32_dpp v64, v85, v102 row_newbcast:9 row_mask:0xf bank_mask:0xc
	s_cselect_b64 s[22:23], -1, 0
	v_cmp_lt_i32_e64 s[6:7], 12, v108
	s_waitcnt lgkmcnt(1)
	v_mfma_f32_16x16x32_f16 v[48:51], v[60:63], v[56:59], v[52:55]
	v_add_u32_dpp v32, v85, v102 row_newbcast:2 row_mask:0xf bank_mask:0x3
	v_add_u32_dpp v32, v85, v102 row_newbcast:10 row_mask:0xf bank_mask:0xc
	s_nop 0
	ds_read_b128 v[76:79], v64 offset:52240
	ds_read_b128 v[72:75], v32 offset:52240
	v_add_u32_dpp v32, v85, v102 row_newbcast:3 row_mask:0xf bank_mask:0x3
	v_add_u32_dpp v32, v85, v102 row_newbcast:11 row_mask:0xf bank_mask:0xc
	v_add_u32_dpp v52, v85, v102 row_newbcast:4 row_mask:0xf bank_mask:0x3
	v_add_u32_dpp v52, v85, v102 row_newbcast:12 row_mask:0xf bank_mask:0xc
	ds_read_b128 v[80:83], v32 offset:52240
	ds_read_b128 v[52:55], v52 offset:52240
	v_add_u32_dpp v56, v85, v102 row_newbcast:5 row_mask:0xf bank_mask:0x3
	v_add_u32_dpp v56, v85, v102 row_newbcast:13 row_mask:0xf bank_mask:0xc
	v_add_u32_dpp v57, v85, v102 row_newbcast:6 row_mask:0xf bank_mask:0x3
	v_add_u32_dpp v57, v85, v102 row_newbcast:14 row_mask:0xf bank_mask:0xc
	ds_read_b128 v[60:63], v56 offset:52240
	ds_read_b128 v[64:67], v57 offset:52240
	v_add_u32_dpp v32, v85, v102 row_newbcast:7 row_mask:0xf bank_mask:0x3
	v_add_u32_dpp v32, v85, v102 row_newbcast:15 row_mask:0xf bank_mask:0xc
	ds_read_b128 v[56:59], v32 offset:52240
	s_cbranch_vccz .LBB4_63
	v_add_u32_dpp v0, v84, v102 row_newbcast:0 row_mask:0xf bank_mask:0x3
	v_add_u32_dpp v0, v84, v102 row_newbcast:8 row_mask:0xf bank_mask:0xc
	v_add_u32_dpp v8, v84, v102 row_newbcast:1 row_mask:0xf bank_mask:0x3
	v_add_u32_dpp v8, v84, v102 row_newbcast:9 row_mask:0xf bank_mask:0xc
	v_add_u32_dpp v16, v84, v102 row_newbcast:2 row_mask:0xf bank_mask:0x3
	v_add_u32_dpp v16, v84, v102 row_newbcast:10 row_mask:0xf bank_mask:0xc
	v_add_u32_dpp v24, v84, v102 row_newbcast:3 row_mask:0xf bank_mask:0x3
	v_add_u32_dpp v24, v84, v102 row_newbcast:11 row_mask:0xf bank_mask:0xc
	ds_read_b128 v[0:3], v0 offset:52240
	ds_read_b128 v[8:11], v8 offset:52240
	ds_read_b128 v[16:19], v16 offset:52240
	ds_read_b128 v[24:27], v24 offset:52240

.LBB4_80:
	ds_write_b128 v104, v[68:71]
	ds_read_b128 v[52:55], v105 offset:128
	ds_read_b128 v[56:59], v103
	ds_read_b128 v[60:63], v105 offset:8832
	s_waitcnt lgkmcnt(1)
	v_mfma_f32_16x16x32_f16 v[36:39], v[52:55], v[56:59], v[36:39]
	ds_read_b128 v[52:55], v105 offset:17536
	s_waitcnt lgkmcnt(1)
	v_mfma_f32_16x16x32_f16 v[40:43], v[60:63], v[56:59], v[40:43]
	s_waitcnt lgkmcnt(0)
	v_mfma_f32_16x16x32_f16 v[44:47], v[52:55], v[56:59], v[44:47]
	ds_read_b128 v[52:55], v105 offset:26240
	s_waitcnt lgkmcnt(0)
	v_mfma_f32_16x16x32_f16 v[48:51], v[52:55], v[56:59], v[48:51]
	ds_read_b128 v[52:55], v105 offset:192
	ds_read_b128 v[56:59], v103 offset:64
	ds_read_b128 v[60:63], v105 offset:8896
	v_cmp_lt_i32_e32 vcc, 8, v35
	s_waitcnt lgkmcnt(1)
	v_mfma_f32_16x16x32_f16 v[36:39], v[52:55], v[56:59], v[36:39]
	ds_read_b128 v[52:55], v105 offset:17600
	v_add_u32_dpp v32, v107, v102 row_newbcast:0 row_mask:0xf bank_mask:0x3
	v_add_u32_dpp v32, v107, v102 row_newbcast:8 row_mask:0xf bank_mask:0xc
	ds_read_b128 v[68:71], v32 offset:52240
	s_waitcnt lgkmcnt(2)
	v_mfma_f32_16x16x32_f16 v[40:43], v[60:63], v[56:59], v[40:43]
	ds_read_b128 v[60:63], v105 offset:26304
	v_add_u32_dpp v33, v107, v102 row_newbcast:1 row_mask:0xf bank_mask:0x3
	v_add_u32_dpp v33, v107, v102 row_newbcast:9 row_mask:0xf bank_mask:0xc
	s_cmp_lg_u64 vcc, 0
	s_waitcnt lgkmcnt(2)
	v_mfma_f32_16x16x32_f16 v[44:47], v[52:55], v[56:59], v[44:47]
	v_add_u32_dpp v32, v107, v102 row_newbcast:2 row_mask:0xf bank_mask:0x3
	v_add_u32_dpp v32, v107, v102 row_newbcast:10 row_mask:0xf bank_mask:0xc
	ds_read_b128 v[76:79], v33 offset:52240
	ds_read_b128 v[72:75], v32 offset:52240
	s_waitcnt lgkmcnt(2)
	v_mfma_f32_16x16x32_f16 v[48:51], v[60:63], v[56:59], v[48:51]
	v_add_u32_dpp v32, v107, v102 row_newbcast:3 row_mask:0xf bank_mask:0x3
	v_add_u32_dpp v32, v107, v102 row_newbcast:11 row_mask:0xf bank_mask:0xc
	v_add_u32_dpp v33, v107, v102 row_newbcast:4 row_mask:0xf bank_mask:0x3
	v_add_u32_dpp v33, v107, v102 row_newbcast:12 row_mask:0xf bank_mask:0xc
	ds_read_b128 v[80:83], v32 offset:52240
	ds_read_b128 v[52:55], v33 offset:52240
	s_cselect_b64 s[22:23], -1, 0
	v_add_u32_dpp v33, v107, v102 row_newbcast:5 row_mask:0xf bank_mask:0x3
	v_add_u32_dpp v33, v107, v102 row_newbcast:13 row_mask:0xf bank_mask:0xc
	v_add_u32_dpp v56, v107, v102 row_newbcast:6 row_mask:0xf bank_mask:0x3
	v_add_u32_dpp v56, v107, v102 row_newbcast:14 row_mask:0xf bank_mask:0xc
	ds_read_b128 v[60:63], v33 offset:52240
	ds_read_b128 v[64:67], v56 offset:52240
	v_add_u32_dpp v32, v107, v102 row_newbcast:7 row_mask:0xf bank_mask:0x3
	v_add_u32_dpp v32, v107, v102 row_newbcast:15 row_mask:0xf bank_mask:0xc
	ds_read_b128 v[56:59], v32 offset:52240
	v_cmp_lt_i32_e64 s[6:7], 12, v35
	s_cbranch_vccz .LBB4_82
	v_add_u32_dpp v0, v106, v102 row_newbcast:0 row_mask:0xf bank_mask:0x3
	v_add_u32_dpp v0, v106, v102 row_newbcast:8 row_mask:0xf bank_mask:0xc
	v_add_u32_dpp v8, v106, v102 row_newbcast:1 row_mask:0xf bank_mask:0x3
	v_add_u32_dpp v8, v106, v102 row_newbcast:9 row_mask:0xf bank_mask:0xc
	v_add_u32_dpp v16, v106, v102 row_newbcast:2 row_mask:0xf bank_mask:0x3
	v_add_u32_dpp v16, v106, v102 row_newbcast:10 row_mask:0xf bank_mask:0xc
	v_add_u32_dpp v24, v106, v102 row_newbcast:3 row_mask:0xf bank_mask:0x3
	v_add_u32_dpp v24, v106, v102 row_newbcast:11 row_mask:0xf bank_mask:0xc
	ds_read_b128 v[0:3], v0 offset:52240
	ds_read_b128 v[8:11], v8 offset:52240
	ds_read_b128 v[16:19], v16 offset:52240
	ds_read_b128 v[24:27], v24 offset:52240

.LBB4_99:
	ds_write_b128 v104, v[68:71]
	ds_read_b128 v[32:35], v105 offset:256
	ds_read_b128 v[52:55], v103
	ds_read_b128 v[56:59], v105 offset:8960
	s_waitcnt lgkmcnt(1)
	v_mfma_f32_16x16x32_f16 v[32:35], v[32:35], v[52:55], v[36:39]
	s_nop 2
	ds_read_b128 v[36:39], v105 offset:17664
	s_waitcnt lgkmcnt(1)
	v_mfma_f32_16x16x32_f16 v[40:43], v[56:59], v[52:55], v[40:43]
	s_waitcnt lgkmcnt(0)
	v_mfma_f32_16x16x32_f16 v[44:47], v[36:39], v[52:55], v[44:47]
	ds_read_b128 v[36:39], v105 offset:26368
	s_waitcnt lgkmcnt(0)
	v_mfma_f32_16x16x32_f16 v[52:55], v[36:39], v[52:55], v[48:51]
	ds_read_b128 v[36:39], v105 offset:320
	ds_read_b128 v[56:59], v103 offset:64
	s_nop 0
	ds_read_b128 v[48:51], v105 offset:9024
	ds_read_b128 v[60:63], v105 offset:17728
	ds_read_b128 v[64:67], v105 offset:26432
	s_waitcnt lgkmcnt(3)
	v_mfma_f32_16x16x32_f16 v[32:35], v[36:39], v[56:59], v[32:35]
	s_waitcnt lgkmcnt(2)
	v_mfma_f32_16x16x32_f16 v[36:39], v[48:51], v[56:59], v[40:43]
	v_mov_b32_e32 v48, 0
	v_mov_b32_e32 v49, v48
	v_mov_b32_e32 v50, v48
	s_waitcnt lgkmcnt(1)
	v_mfma_f32_16x16x32_f16 v[40:43], v[60:63], v[56:59], v[44:47]
	v_mov_b32_e32 v51, v48
	s_waitcnt lgkmcnt(0)
	v_mfma_f32_16x16x32_f16 v[44:47], v[64:67], v[56:59], v[52:55]
	s_and_saveexec_b64 s[6:7], s[4:5]
	s_cbranch_execz .LBB4_101
	v_lshlrev_b32_e32 v48, 7, v114
	v_lshl_add_u32 v49, v115, 11, 0
	v_add3_u32 v48, v49, v48, v98
	ds_read_b128 v[48:51], v48 offset:52240
.LBB4_101:
	s_or_b64 exec, exec, s[6:7]
	s_waitcnt lgkmcnt(0)
	ds_write_b128 v104, v[48:51]
	ds_read_b128 v[48:51], v105 offset:384
	ds_read_b128 v[52:55], v103
	ds_read_b128 v[56:59], v105 offset:9088
	s_waitcnt lgkmcnt(1)
	v_mfma_f32_16x16x32_f16 v[32:35], v[48:51], v[52:55], v[32:35]
	ds_read_b128 v[48:51], v105 offset:17792
	s_waitcnt lgkmcnt(1)
	v_mfma_f32_16x16x32_f16 v[36:39], v[56:59], v[52:55], v[36:39]
	s_waitcnt lgkmcnt(0)
	v_mfma_f32_16x16x32_f16 v[56:59], v[48:51], v[52:55], v[40:43]
	s_nop 2
	ds_read_b128 v[40:43], v105 offset:26496
	s_waitcnt lgkmcnt(0)
	v_mfma_f32_16x16x32_f16 v[50:53], v[40:43], v[52:55], v[44:47]
	ds_read_b128 v[40:43], v105 offset:448
	ds_read_b128 v[60:63], v103 offset:64
	ds_read_b128 v[64:67], v105 offset:9152
	v_add_u32_e32 v48, s19, v99
	v_cmp_gt_i32_e32 vcc, s18, v48
	s_and_b64 s[4:5], s[2:3], vcc
	s_waitcnt lgkmcnt(1)
	v_mfma_f32_16x16x32_f16 v[44:47], v[40:43], v[60:63], v[32:35]
	s_mov_b64 s[6:7], s[20:21]
	s_mov_b64 s[22:23], s[24:25]
	s_nop 0
	ds_read_b128 v[32:35], v105 offset:17856
	s_waitcnt lgkmcnt(1)
	v_mfma_f32_16x16x32_f16 v[40:43], v[64:67], v[60:63], v[36:39]
	ds_read_b128 v[64:67], v105 offset:26560
	s_waitcnt lgkmcnt(1)
	v_mfma_f32_16x16x32_f16 v[36:39], v[32:35], v[60:63], v[56:59]
	s_waitcnt lgkmcnt(0)
	v_mfma_f32_16x16x32_f16 v[32:35], v[64:67], v[60:63], v[50:53]
	s_and_saveexec_b64 s[22:23], s[4:5]
	s_xor_b64 s[4:5], exec, s[22:23]
	s_cbranch_execz .LBB4_15
	v_add_u32_e32 v50, 0x1cc90, v88
	ds_read_b128 v[52:55], v50
	v_mov_b32_e32 v56, v89
	s_waitcnt lgkmcnt(0)
	v_add_f32_e32 v44, v44, v52
	v_add_f32_e32 v45, v45, v53
	v_max_f32_e32 v57, 0, v44
	v_max_f32_e32 v58, 0, v45
	v_mul_f32_e32 v44, 0x42800000, v57
	v_mul_f32_e32 v45, 0x42800000, v58
	v_min_f32_e32 v44, 0x43e00000, v44
	v_min_f32_e32 v45, 0x43e00000, v45
	v_add_f32_e32 v46, v46, v54
	v_add_f32_e32 v47, v47, v55
	v_cvt_pk_fp8_f32 v56, v44, v45
	v_max_f32_e32 v46, 0, v46
	v_max_f32_e32 v47, 0, v47
	v_mul_f32_e32 v49, 0x42800000, v46
	v_mul_f32_e32 v44, 0x42800000, v47
	v_min_f32_e32 v45, 0x43e00000, v49
	v_min_f32_e32 v44, 0x43e00000, v44
	v_cvt_pk_fp8_f32 v56, v45, v44 op_sel:[0,0,1]
	v_ashrrev_i32_e32 v49, 31, v48
	v_lshlrev_b64 v[44:45], 6, v[48:49]
	v_lshl_add_u64 v[44:45], v[92:93], 0, v[44:45]
	global_store_dword v[44:45], v56, off
	ds_read_b128 v[52:55], v50 offset:64
	v_mov_b32_e32 v56, v89
	s_waitcnt lgkmcnt(0)
	v_add_f32_e32 v40, v40, v52
	v_add_f32_e32 v41, v41, v53
	v_max_f32_e32 v52, 0, v40
	v_max_f32_e32 v53, 0, v41
	v_mul_f32_e32 v40, 0x42800000, v52
	v_mul_f32_e32 v41, 0x42800000, v53
	v_min_f32_e32 v40, 0x43e00000, v40
	v_min_f32_e32 v41, 0x43e00000, v41
	v_add_f32_e32 v42, v42, v54
	v_add_f32_e32 v43, v43, v55
	v_cvt_pk_fp8_f32 v56, v40, v41
	v_max_f32_e32 v54, 0, v42
	v_max_f32_e32 v55, 0, v43
	v_mul_f32_e32 v42, 0x42800000, v54
	v_mul_f32_e32 v40, 0x42800000, v55
	v_min_f32_e32 v41, 0x43e00000, v42
	v_min_f32_e32 v40, 0x43e00000, v40
	v_cvt_pk_fp8_f32 v56, v41, v40 op_sel:[0,0,1]
	global_store_dword v[44:45], v56, off offset:16
	ds_read_b128 v[40:43], v50 offset:128
	v_mov_b32_e32 v56, v89
	s_waitcnt lgkmcnt(0)
	v_add_f32_e32 v36, v36, v40
	v_add_f32_e32 v37, v37, v41
	v_max_f32_e32 v59, 0, v36
	v_max_f32_e32 v60, 0, v37
	v_mul_f32_e32 v36, 0x42800000, v59
	v_mul_f32_e32 v37, 0x42800000, v60
	v_min_f32_e32 v36, 0x43e00000, v36
	v_min_f32_e32 v37, 0x43e00000, v37
	v_add_f32_e32 v38, v38, v42
	v_add_f32_e32 v39, v39, v43
	v_cvt_pk_fp8_f32 v56, v36, v37
	v_max_f32_e32 v61, 0, v38
	v_max_f32_e32 v62, 0, v39
	v_mul_f32_e32 v38, 0x42800000, v61
	v_mul_f32_e32 v36, 0x42800000, v62
	v_min_f32_e32 v37, 0x43e00000, v38
	v_min_f32_e32 v36, 0x43e00000, v36
	v_cvt_pk_fp8_f32 v56, v37, v36 op_sel:[0,0,1]
	v_lshlrev_b64 v[40:41], 7, v[48:49]
	v_lshl_add_u64 v[40:41], v[90:91], 0, v[40:41]
	v_cvt_pk_f16_f32 v43, v46, v47
	global_store_dword v[44:45], v56, off offset:32
	ds_read_b128 v[36:39], v50 offset:192
	v_cvt_pk_f16_f32 v42, v57, v58
	global_store_dwordx2 v[40:41], v[42:43], off
	v_cvt_pk_f16_f32 v43, v54, v55
	v_cvt_pk_f16_f32 v42, v52, v53
	global_store_dwordx2 v[40:41], v[42:43], off offset:32
	v_cvt_pk_f16_f32 v43, v61, v62
	v_cvt_pk_f16_f32 v42, v59, v60
	global_store_dwordx2 v[40:41], v[42:43], off offset:64
	s_waitcnt lgkmcnt(0)
	v_add_f32_e32 v32, v32, v36
	v_add_f32_e32 v33, v33, v37
	v_add_f32_e32 v34, v34, v38
	v_add_f32_e32 v35, v35, v39
	v_max_f32_e32 v32, 0, v32
	v_max_f32_e32 v36, 0, v33
	v_max_f32_e32 v33, 0, v34
	v_max_f32_e32 v34, 0, v35
	v_mul_f32_e32 v35, 0x42800000, v32
	v_mul_f32_e32 v37, 0x42800000, v36
	v_min_f32_e32 v35, 0x43e00000, v35
	v_min_f32_e32 v37, 0x43e00000, v37
	v_mov_b32_e32 v39, v89
	v_cvt_pk_fp8_f32 v39, v35, v37
	v_mul_f32_e32 v38, 0x42800000, v33
	v_mul_f32_e32 v37, 0x42800000, v34
	v_min_f32_e32 v35, 0x43e00000, v38
	v_min_f32_e32 v37, 0x43e00000, v37
	v_cvt_pk_fp8_f32 v39, v35, v37 op_sel:[0,0,1]
	v_cvt_pk_f16_f32 v33, v33, v34
	v_cvt_pk_f16_f32 v32, v32, v36
	global_store_dwordx2 v[40:41], v[32:33], off offset:96
	global_store_dword v[44:45], v39, off offset:48
	s_branch .LBB4_15

.LBB5_10:
	v_lshrrev_b32_e32 v2, 3, v0
	s_load_dwordx2 s[30:31], s[0:1], 0x40
	v_and_b32_e32 v1, 63, v0
	v_and_b32_e32 v2, 0x78, v2
	s_movk_i32 s2, 0xa0
	v_bfe_u32 v74, v0, 3, 3
	v_and_b32_e32 v75, 7, v0
	v_and_b32_e32 v77, 15, v0
	s_sub_i32 s0, s28, s20
	v_and_b32_e32 v5, 48, v0
	v_lshrrev_b32_e32 v0, 2, v0
	v_mad_u32_u24 v2, v2, s2, 0
	s_add_i32 s0, s0, 7
	v_mul_u32_u24_e32 v4, 0xa0, v75
	v_and_b32_e32 v0, 12, v0
	v_lshlrev_b32_e32 v76, 4, v75
	s_ashr_i32 s21, s0, 3
	v_cmp_eq_u32_e64 s[0:1], 0, v1
	v_mad_u32_u24 v3, v74, s2, v2
	v_add3_u32 v80, v2, v4, v5
	v_add_u32_e32 v2, 0, v5
	v_cmp_gt_u32_e64 s[4:5], 16, v1
	v_mul_u32_u24_e32 v1, 0x220, v77
	v_lshlrev_b32_e32 v32, 2, v0
	v_mbcnt_lo_u32_b32 v0, -1, 0
	v_mov_b32_e32 v33, 0
	v_or_b32_e32 v78, 8, v75
	v_or_b32_e32 v79, 16, v75
	v_lshlrev_b32_e32 v81, 3, v75
	v_cmp_gt_u32_e64 s[2:3], 8, v77
	s_mov_b32 s29, 0x3c800000
	v_add_u32_e32 v82, v3, v76
	v_add_u32_e32 v83, v2, v1
	v_add_u32_e32 v83, 0xcf10, v83
	v_mbcnt_hi_u32_b32 v84, -1, v0
	s_lshl_b32 s33, s38, 3
	s_add_i32 s33, s33, s20
	v_add_u32_e32 v8, s33, v74
	v_cmp_gt_i32_e32 vcc, s28, v8
	v_mov_b32_e32 v0, 0
	v_mov_b32_e32 v1, 0
	v_mov_b32_e32 v2, 0
	v_mov_b32_e32 v3, 0
	v_mov_b32_e32 v4, 0
	v_mov_b32_e32 v5, 0
	v_mov_b32_e32 v6, 0
	v_mov_b32_e32 v7, 0
	s_and_saveexec_b64 s[6:7], vcc
	v_lshl_add_u32 v9, v8, 1, v8
	v_lshlrev_b32_e32 v9, 2, v9
	global_load_dwordx4 v[4:7], v9, s[14:15]
	v_lshl_or_b32 v9, v8, 7, v76
	global_load_dwordx4 v[0:3], v9, s[12:13]
	s_mov_b64 exec, s[6:7]
	s_waitcnt vmcnt(3)
	ds_write_b128 v20, v[22:25]
	s_waitcnt vmcnt(2)
	ds_write_b128 v20, v[26:29] offset:17408
	s_and_saveexec_b64 s[6:7], s[40:41]
	ds_write_b128 v14, v[16:19] offset:52240
	s_mov_b64 exec, s[6:7]
	s_waitcnt vmcnt(1)
	v_sub_u32_e32 v58, v5, v4
	v_sub_u32_e32 v87, v6, v5
	v_sub_u32_e32 v85, v7, v6
	v_add_lshl_u32 v10, v4, v75, 2
	v_add_lshl_u32 v11, v5, v75, 2
	v_add_lshl_u32 v12, v6, v75, 2
	v_mov_b32_e32 v9, 0x186a0
	v_mov_b32_e32 v8, 0x186a0
	v_mov_b32_e32 v60, 0x186a0
	v_mov_b32_e32 v59, 0x186a0
	v_mov_b32_e32 v62, 0x186a0
	v_mov_b32_e32 v89, 0x186a0
	v_mov_b32_e32 v88, 0x186a0
	v_mov_b32_e32 v86, 0x186a0
	v_mov_b32_e32 v7, 0x186a0
	s_mov_b64 s[6:7], exec
	v_cmp_lt_i32_e32 vcc, v75, v58
	s_and_b64 exec, exec, vcc
	global_load_dword v9, v10, s[26:27]
	v_cmp_lt_i32_e32 vcc, v78, v58
	s_and_b64 exec, exec, vcc
	global_load_dword v8, v10, s[26:27] offset:32
	v_cmp_lt_i32_e32 vcc, v79, v58
	s_and_b64 exec, exec, vcc
	global_load_dword v60, v10, s[26:27] offset:64
	s_mov_b64 exec, s[6:7]
	v_cmp_lt_i32_e32 vcc, v75, v87
	s_and_b64 exec, exec, vcc
	global_load_dword v59, v11, s[26:27]
	v_cmp_lt_i32_e32 vcc, v78, v87
	s_and_b64 exec, exec, vcc
	global_load_dword v62, v11, s[26:27] offset:32
	v_cmp_lt_i32_e32 vcc, v79, v87
	s_and_b64 exec, exec, vcc
	global_load_dword v89, v11, s[26:27] offset:64
	s_mov_b64 exec, s[6:7]
	v_cmp_lt_i32_e32 vcc, v75, v85
	s_and_b64 exec, exec, vcc
	global_load_dword v88, v12, s[26:27]
	v_cmp_lt_i32_e32 vcc, v78, v85
	s_and_b64 exec, exec, vcc
	global_load_dword v86, v12, s[26:27] offset:32
	v_cmp_lt_i32_e32 vcc, v79, v85
	s_and_b64 exec, exec, vcc
	global_load_dword v7, v12, s[26:27] offset:64
	s_mov_b64 exec, s[6:7]
	s_waitcnt lgkmcnt(0)
	s_barrier
	s_cmp_ge_i32 s38, s21
	s_cbranch_scc1 .LBB5_118
	s_branch .Lp2_after_idx

.LBB5_61:
	s_cbranch_execz .LBB5_58
	ds_write_b128 v82, v[8:11]
	ds_read_b128 v[8:11], v83
	ds_read_b128 v[12:15], v80
	ds_read_b128 v[16:19], v83 offset:8704
	ds_read_b128 v[20:23], v83 offset:17408
	ds_read_b128 v[24:27], v83 offset:26112
	s_waitcnt lgkmcnt(3)
	v_mfma_f32_16x16x32_f16 v[8:11], v[8:11], v[12:15], 0
	s_waitcnt lgkmcnt(2)
	v_mfma_f32_16x16x32_f16 v[16:19], v[16:19], v[12:15], 0
	s_waitcnt lgkmcnt(1)
	v_mfma_f32_16x16x32_f16 v[20:23], v[20:23], v[12:15], 0
	s_waitcnt lgkmcnt(0)
	v_mfma_f32_16x16x32_f16 v[90:93], v[24:27], v[12:15], 0
	ds_read_b128 v[12:15], v83 offset:64
	ds_read_b128 v[94:97], v80 offset:64
	ds_read_b128 v[24:27], v83 offset:8768
	ds_read_b128 v[98:101], v83 offset:17472
	s_waitcnt lgkmcnt(2)
	v_mfma_f32_16x16x32_f16 v[8:11], v[12:15], v[94:97], v[8:11]
	v_add_u32_dpp v4, v59, v81 row_newbcast:0 row_mask:0xf bank_mask:0x3
	v_add_u32_dpp v4, v59, v81 row_newbcast:8 row_mask:0xf bank_mask:0xc
	s_waitcnt lgkmcnt(1)
	v_mfma_f32_16x16x32_f16 v[12:15], v[24:27], v[94:97], v[16:19]
	v_mov_b32_dpp v24, v59 row_newbcast:5 row_mask:0xf bank_mask:0x3
	v_mov_b32_dpp v24, v59 row_newbcast:13 row_mask:0xf bank_mask:0xc
	v_mov_b32_dpp v25, v59 row_newbcast:6 row_mask:0xf bank_mask:0x3
	v_mov_b32_dpp v25, v59 row_newbcast:14 row_mask:0xf bank_mask:0xc
	v_mov_b32_dpp v26, v59 row_newbcast:7 row_mask:0xf bank_mask:0x3
	v_mov_b32_dpp v26, v59 row_newbcast:15 row_mask:0xf bank_mask:0xc
	v_mov_b32_dpp v19, v59 row_newbcast:4 row_mask:0xf bank_mask:0x3
	v_mov_b32_dpp v19, v59 row_newbcast:12 row_mask:0xf bank_mask:0xc
	v_add_u32_dpp v16, v59, v81 row_newbcast:1 row_mask:0xf bank_mask:0x3
	v_add_u32_dpp v16, v59, v81 row_newbcast:9 row_mask:0xf bank_mask:0xc
	v_add_u32_dpp v17, v59, v81 row_newbcast:2 row_mask:0xf bank_mask:0x3
	v_add_u32_dpp v17, v59, v81 row_newbcast:10 row_mask:0xf bank_mask:0xc
	v_add_u32_dpp v18, v59, v81 row_newbcast:3 row_mask:0xf bank_mask:0x3
	v_add_u32_dpp v18, v59, v81 row_newbcast:11 row_mask:0xf bank_mask:0xc
	global_load_dwordx2 v[72:73], v4, s[30:31]
	global_load_dwordx2 v[68:69], v16, s[30:31]
	global_load_dwordx2 v[64:65], v17, s[30:31]
	global_load_dwordx2 v[58:59], v18, s[30:31]
	v_add_u32_e32 v4, v19, v81
	v_add_u32_e32 v16, v24, v81
	v_add_u32_e32 v17, v25, v81
	v_add_u32_e32 v18, v26, v81
	global_load_dwordx2 v[70:71], v4, s[30:31]
	global_load_dwordx2 v[66:67], v16, s[30:31]
	global_load_dwordx2 v[60:61], v17, s[30:31]
	global_load_dwordx2 v[54:55], v18, s[30:31]
	v_add_u32_dpp v4, v62, v81 row_newbcast:0 row_mask:0xf bank_mask:0x3
	v_add_u32_dpp v4, v62, v81 row_newbcast:8 row_mask:0xf bank_mask:0xc
	v_mov_b32_dpp v19, v62 row_newbcast:4 row_mask:0xf bank_mask:0x3
	v_mov_b32_dpp v19, v62 row_newbcast:12 row_mask:0xf bank_mask:0xc
	v_add_u32_dpp v16, v62, v81 row_newbcast:1 row_mask:0xf bank_mask:0x3
	v_add_u32_dpp v16, v62, v81 row_newbcast:9 row_mask:0xf bank_mask:0xc
	v_add_u32_dpp v17, v62, v81 row_newbcast:2 row_mask:0xf bank_mask:0x3
	v_add_u32_dpp v17, v62, v81 row_newbcast:10 row_mask:0xf bank_mask:0xc
	v_add_u32_dpp v18, v62, v81 row_newbcast:3 row_mask:0xf bank_mask:0x3
	v_add_u32_dpp v18, v62, v81 row_newbcast:11 row_mask:0xf bank_mask:0xc
	v_mov_b32_dpp v24, v62 row_newbcast:5 row_mask:0xf bank_mask:0x3
	v_mov_b32_dpp v24, v62 row_newbcast:13 row_mask:0xf bank_mask:0xc
	v_mov_b32_dpp v25, v62 row_newbcast:6 row_mask:0xf bank_mask:0x3
	v_mov_b32_dpp v25, v62 row_newbcast:14 row_mask:0xf bank_mask:0xc
	v_mov_b32_dpp v26, v62 row_newbcast:7 row_mask:0xf bank_mask:0x3
	v_mov_b32_dpp v26, v62 row_newbcast:15 row_mask:0xf bank_mask:0xc
	global_load_dwordx2 v[62:63], v4, s[30:31]
	global_load_dwordx2 v[56:57], v16, s[30:31]
	global_load_dwordx2 v[52:53], v17, s[30:31]
	global_load_dwordx2 v[50:51], v18, s[30:31]
	v_add_u32_e32 v4, v19, v81
	v_add_u32_e32 v16, v24, v81
	v_add_u32_e32 v17, v25, v81
	v_add_u32_e32 v18, v26, v81
	global_load_dwordx2 v[30:31], v4, s[30:31]
	global_load_dwordx2 v[28:29], v16, s[30:31]
	global_load_dwordx2 v[26:27], v17, s[30:31]
	global_load_dwordx2 v[24:25], v18, s[30:31]
	s_waitcnt lgkmcnt(0)
	v_mfma_f32_16x16x32_f16 v[16:19], v[98:101], v[94:97], v[20:23]
	v_cmp_lt_i32_e32 vcc, 16, v87
	s_cmp_lg_u64 vcc, 0
	s_cselect_b64 s[36:37], -1, 0
	ds_read_b128 v[20:23], v83 offset:26176
	s_waitcnt lgkmcnt(0)
	v_mfma_f32_16x16x32_f16 v[20:23], v[20:23], v[94:97], v[90:93]
	v_cmp_lt_i32_e64 s[10:11], 18, v87
	v_cmp_lt_i32_e64 s[8:9], 20, v87
	v_cmp_lt_i32_e64 s[6:7], 22, v87
	s_cbranch_vccz .LBB5_64
	v_add_u32_dpp v4, v89, v81 row_newbcast:0 row_mask:0xf bank_mask:0x3
	v_add_u32_dpp v4, v89, v81 row_newbcast:8 row_mask:0xf bank_mask:0xc
	v_add_u32_dpp v38, v89, v81 row_newbcast:1 row_mask:0xf bank_mask:0x3
	v_add_u32_dpp v38, v89, v81 row_newbcast:9 row_mask:0xf bank_mask:0xc
	global_load_dwordx2 v[34:35], v4, s[30:31]
	s_nop 0
	global_load_dwordx2 v[38:39], v38, s[30:31]

.LBB5_83:
	s_cbranch_execz .LBB5_80
	ds_write_b128 v82, v[24:27]
	ds_read_b128 v[24:27], v83 offset:128
	ds_read_b128 v[28:31], v80
	ds_read_b128 v[50:53], v83 offset:8832
	s_waitcnt lgkmcnt(1)
	v_mfma_f32_16x16x32_f16 v[8:11], v[24:27], v[28:31], v[8:11]
	ds_read_b128 v[24:27], v83 offset:17536
	s_waitcnt lgkmcnt(1)
	v_mfma_f32_16x16x32_f16 v[12:15], v[50:53], v[28:31], v[12:15]
	s_waitcnt lgkmcnt(0)
	v_mfma_f32_16x16x32_f16 v[16:19], v[24:27], v[28:31], v[16:19]
	ds_read_b128 v[24:27], v83 offset:26240
	s_waitcnt lgkmcnt(0)
	v_mfma_f32_16x16x32_f16 v[20:23], v[24:27], v[28:31], v[20:23]
	ds_read_b128 v[24:27], v83 offset:192
	ds_read_b128 v[90:93], v80 offset:64
	ds_read_b128 v[28:31], v83 offset:8896
	ds_read_b128 v[94:97], v83 offset:17600
	s_waitcnt lgkmcnt(2)
	v_mfma_f32_16x16x32_f16 v[8:11], v[24:27], v[90:93], v[8:11]
	s_waitcnt lgkmcnt(1)
	v_mfma_f32_16x16x32_f16 v[12:15], v[28:31], v[90:93], v[12:15]
	v_add_u32_dpp v4, v88, v81 row_newbcast:0 row_mask:0xf bank_mask:0x3
	v_add_u32_dpp v4, v88, v81 row_newbcast:8 row_mask:0xf bank_mask:0xc
	v_add_u32_dpp v5, v88, v81 row_newbcast:1 row_mask:0xf bank_mask:0x3
	v_add_u32_dpp v5, v88, v81 row_newbcast:9 row_mask:0xf bank_mask:0xc
	v_add_u32_dpp v24, v88, v81 row_newbcast:2 row_mask:0xf bank_mask:0x3
	v_add_u32_dpp v24, v88, v81 row_newbcast:10 row_mask:0xf bank_mask:0xc
	v_add_u32_dpp v25, v88, v81 row_newbcast:3 row_mask:0xf bank_mask:0x3
	v_add_u32_dpp v25, v88, v81 row_newbcast:11 row_mask:0xf bank_mask:0xc
	global_load_dwordx2 v[70:71], v4, s[30:31]
	global_load_dwordx2 v[66:67], v5, s[30:31]
	global_load_dwordx2 v[62:63], v24, s[30:31]
	global_load_dwordx2 v[56:57], v25, s[30:31]
	v_add_u32_dpp v4, v88, v81 row_newbcast:4 row_mask:0xf bank_mask:0x3
	v_add_u32_dpp v4, v88, v81 row_newbcast:12 row_mask:0xf bank_mask:0xc
	v_add_u32_dpp v5, v88, v81 row_newbcast:5 row_mask:0xf bank_mask:0x3
	v_add_u32_dpp v5, v88, v81 row_newbcast:13 row_mask:0xf bank_mask:0xc
	v_add_u32_dpp v24, v88, v81 row_newbcast:6 row_mask:0xf bank_mask:0x3
	v_add_u32_dpp v24, v88, v81 row_newbcast:14 row_mask:0xf bank_mask:0xc
	v_add_u32_dpp v25, v88, v81 row_newbcast:7 row_mask:0xf bank_mask:0x3
	v_add_u32_dpp v25, v88, v81 row_newbcast:15 row_mask:0xf bank_mask:0xc
	global_load_dwordx2 v[68:69], v4, s[30:31]
	global_load_dwordx2 v[64:65], v5, s[30:31]
	global_load_dwordx2 v[58:59], v24, s[30:31]
	global_load_dwordx2 v[52:53], v25, s[30:31]
	v_add_u32_dpp v4, v86, v81 row_newbcast:0 row_mask:0xf bank_mask:0x3
	v_add_u32_dpp v4, v86, v81 row_newbcast:8 row_mask:0xf bank_mask:0xc
	v_add_u32_dpp v5, v86, v81 row_newbcast:1 row_mask:0xf bank_mask:0x3
	v_add_u32_dpp v5, v86, v81 row_newbcast:9 row_mask:0xf bank_mask:0xc
	v_add_u32_dpp v24, v86, v81 row_newbcast:2 row_mask:0xf bank_mask:0x3
	v_add_u32_dpp v24, v86, v81 row_newbcast:10 row_mask:0xf bank_mask:0xc
	v_add_u32_dpp v25, v86, v81 row_newbcast:3 row_mask:0xf bank_mask:0x3
	v_add_u32_dpp v25, v86, v81 row_newbcast:11 row_mask:0xf bank_mask:0xc
	global_load_dwordx2 v[60:61], v4, s[30:31]
	global_load_dwordx2 v[54:55], v5, s[30:31]
	global_load_dwordx2 v[50:51], v24, s[30:31]
	global_load_dwordx2 v[30:31], v25, s[30:31]
	v_add_u32_dpp v4, v86, v81 row_newbcast:4 row_mask:0xf bank_mask:0x3
	v_add_u32_dpp v4, v86, v81 row_newbcast:12 row_mask:0xf bank_mask:0xc
	v_add_u32_dpp v5, v86, v81 row_newbcast:5 row_mask:0xf bank_mask:0x3
	v_add_u32_dpp v5, v86, v81 row_newbcast:13 row_mask:0xf bank_mask:0xc
	v_add_u32_dpp v24, v86, v81 row_newbcast:6 row_mask:0xf bank_mask:0x3
	v_add_u32_dpp v24, v86, v81 row_newbcast:14 row_mask:0xf bank_mask:0xc
	v_add_u32_dpp v72, v86, v81 row_newbcast:7 row_mask:0xf bank_mask:0x3
	v_add_u32_dpp v72, v86, v81 row_newbcast:15 row_mask:0xf bank_mask:0xc
	global_load_dwordx2 v[28:29], v4, s[30:31]
	global_load_dwordx2 v[26:27], v5, s[30:31]
	s_nop 0
	global_load_dwordx2 v[24:25], v24, s[30:31]
	s_nop 0
	global_load_dwordx2 v[4:5], v72, s[30:31]
	ds_read_b128 v[86:89], v83 offset:26304
	s_waitcnt lgkmcnt(1)
	v_mfma_f32_16x16x32_f16 v[16:19], v[94:97], v[90:93], v[16:19]
	v_cmp_lt_i32_e32 vcc, 16, v85
	s_cmp_lg_u64 vcc, 0
	s_cselect_b64 s[36:37], -1, 0
	s_waitcnt lgkmcnt(0)
	v_mfma_f32_16x16x32_f16 v[20:23], v[86:89], v[90:93], v[20:23]
	v_cmp_lt_i32_e64 s[10:11], 18, v85
	v_cmp_lt_i32_e64 s[8:9], 20, v85
	v_cmp_lt_i32_e64 s[6:7], 22, v85
	s_cbranch_vccz .LBB5_86
	v_add_u32_dpp v34, v7, v81 row_newbcast:0 row_mask:0xf bank_mask:0x3
	v_add_u32_dpp v34, v7, v81 row_newbcast:8 row_mask:0xf bank_mask:0xc
	v_add_u32_dpp v38, v7, v81 row_newbcast:1 row_mask:0xf bank_mask:0x3
	v_add_u32_dpp v38, v7, v81 row_newbcast:9 row_mask:0xf bank_mask:0xc
	global_load_dwordx2 v[34:35], v34, s[30:31]
	s_nop 0
	global_load_dwordx2 v[38:39], v38, s[30:31]

.LBB5_105:
	s_cbranch_execz .LBB5_102
	ds_write_b128 v82, v[4:7]
	ds_read_b128 v[4:7], v83 offset:256
	ds_read_b128 v[24:27], v80
	ds_read_b128 v[28:31], v83 offset:8960
	s_waitcnt lgkmcnt(1)
	v_mfma_f32_16x16x32_f16 v[4:7], v[4:7], v[24:27], v[8:11]
	s_nop 2
	ds_read_b128 v[8:11], v83 offset:17664
	s_waitcnt lgkmcnt(1)
	v_mfma_f32_16x16x32_f16 v[12:15], v[28:31], v[24:27], v[12:15]
	s_waitcnt lgkmcnt(0)
	v_mfma_f32_16x16x32_f16 v[8:11], v[8:11], v[24:27], v[16:19]
	s_nop 2
	ds_read_b128 v[16:19], v83 offset:26368
	s_waitcnt lgkmcnt(0)
	v_mfma_f32_16x16x32_f16 v[16:19], v[16:19], v[24:27], v[20:23]
	s_nop 2
	ds_read_b128 v[20:23], v83 offset:320
	ds_read_b128 v[24:27], v80 offset:64
	ds_read_b128 v[28:31], v83 offset:9024
	s_waitcnt lgkmcnt(1)
	v_mfma_f32_16x16x32_f16 v[4:7], v[20:23], v[24:27], v[4:7]
	ds_read_b128 v[20:23], v83 offset:17728
	s_waitcnt lgkmcnt(1)
	v_mfma_f32_16x16x32_f16 v[12:15], v[28:31], v[24:27], v[12:15]
	s_waitcnt lgkmcnt(0)
	v_mfma_f32_16x16x32_f16 v[8:11], v[20:23], v[24:27], v[8:11]
	ds_read_b128 v[20:23], v83 offset:26432
	ds_write_b128 v82, v[0:3]
	s_waitcnt lgkmcnt(1)
	v_mfma_f32_16x16x32_f16 v[0:3], v[20:23], v[24:27], v[16:19]
	s_nop 2
	ds_read_b128 v[16:19], v83 offset:384
	ds_read_b128 v[20:23], v80
	ds_read_b128 v[24:27], v83 offset:9088
	s_waitcnt lgkmcnt(1)
	v_mfma_f32_16x16x32_f16 v[4:7], v[16:19], v[20:23], v[4:7]
	ds_read_b128 v[16:19], v83 offset:17792
	s_waitcnt lgkmcnt(1)
	v_mfma_f32_16x16x32_f16 v[12:15], v[24:27], v[20:23], v[12:15]
	s_waitcnt lgkmcnt(0)
	v_mfma_f32_16x16x32_f16 v[8:11], v[16:19], v[20:23], v[8:11]
	ds_read_b128 v[16:19], v83 offset:26496
	s_waitcnt lgkmcnt(0)
	v_mfma_f32_16x16x32_f16 v[0:3], v[16:19], v[20:23], v[0:3]
	ds_read_b128 v[16:19], v83 offset:448
	ds_read_b128 v[20:23], v80 offset:64
	ds_read_b128 v[24:27], v83 offset:9152
	ds_read_b128 v[28:31], v83 offset:17856
	ds_read_b128 v[50:53], v83 offset:26560
	s_mov_b64 s[6:7], s[22:23]
	s_mov_b64 s[8:9], s[18:19]
	s_waitcnt lgkmcnt(1)
	v_mfma_f32_16x16x32_f16 v[8:11], v[28:31], v[20:23], v[8:11]
	s_nop 0
	s_waitcnt lgkmcnt(0)
	v_mfma_f32_16x16x32_f16 v[0:3], v[50:53], v[20:23], v[0:3]
	v_mfma_f32_16x16x32_f16 v[16:19], v[16:19], v[20:23], v[4:7]
	s_nop 2
	v_add_u32_e32 v6, s33, v77
	v_mfma_f32_16x16x32_f16 v[12:15], v[24:27], v[20:23], v[12:15]
	v_cmp_gt_i32_e32 vcc, s28, v6
	ds_read_b128 v[20:23], v32 offset:52240
	ds_read_b128 v[24:27], v32 offset:52496
	ds_read_b128 v[28:31], v32 offset:52752
	s_waitcnt lgkmcnt(2)
	v_add_f32_e32 v7, v16, v20
	s_waitcnt lgkmcnt(1)
	v_mov_b32_e32 v4, v24
	s_waitcnt lgkmcnt(0)
	v_mov_b32_e32 v5, v28
	v_add_f32_e32 v16, v17, v21
	v_add_f32_e32 v17, v18, v22
	v_add_f32_e32 v18, v19, v23
	v_max_f32_e32 v24, 0, v7
	v_max_f32_e32 v62, 0, v16
	v_max_f32_e32 v64, 0, v17
	v_max_f32_e32 v66, 0, v18
	ds_read_b128 v[16:19], v32 offset:52304
	ds_read_b128 v[20:23], v32 offset:52560
	ds_read_b128 v[50:53], v32 offset:52816
	s_waitcnt lgkmcnt(2)
	v_add_f32_e32 v7, v12, v16
	v_add_f32_e32 v12, v13, v17
	v_add_f32_e32 v13, v14, v18
	v_add_f32_e32 v14, v15, v19
	v_max_f32_e32 v68, 0, v7
	v_max_f32_e32 v70, 0, v12
	v_max_f32_e32 v72, 0, v13
	v_max_f32_e32 v86, 0, v14
	ds_read_b128 v[12:15], v32 offset:52368
	ds_read_b128 v[16:19], v32 offset:52624
	ds_read_b128 v[54:57], v32 offset:52880
	v_pk_fma_f32 v[88:89], v[4:5], v[24:25], 0 op_sel_hi:[1,0,0]
	v_mov_b32_e32 v28, v25
	v_mov_b32_e32 v24, v26
	v_mov_b32_e32 v25, v30
	v_mov_b32_e32 v30, v27
	s_waitcnt lgkmcnt(4)
	v_mov_b32_e32 v26, v20
	s_waitcnt lgkmcnt(3)
	v_mov_b32_e32 v27, v50
	v_mov_b32_e32 v50, v21
	v_mov_b32_e32 v20, v22
	v_mov_b32_e32 v21, v52
	v_mov_b32_e32 v52, v23
	v_pk_fma_f32 v[22:23], v[28:29], v[62:63], v[88:89] op_sel_hi:[1,0,1]
	v_mov_b32_e32 v4, v33
	v_pk_fma_f32 v[22:23], v[24:25], v[64:65], v[22:23] op_sel_hi:[1,0,1]
	v_mov_b32_e32 v5, v33
	v_pk_fma_f32 v[22:23], v[30:31], v[66:67], v[22:23] op_sel_hi:[1,0,1]
	s_waitcnt lgkmcnt(2)
	v_add_f32_e32 v7, v8, v12
	v_pk_fma_f32 v[22:23], v[26:27], v[68:69], v[22:23] op_sel_hi:[1,0,1]
	s_waitcnt lgkmcnt(1)
	v_mov_b32_e32 v8, v16
	v_pk_fma_f32 v[22:23], v[50:51], v[70:71], v[22:23] op_sel_hi:[1,0,1]
	v_add_f32_e32 v11, v11, v15
	v_pk_fma_f32 v[20:21], v[20:21], v[72:73], v[22:23] op_sel_hi:[1,0,1]
	v_add_f32_e32 v22, v9, v13
	v_pk_fma_f32 v[20:21], v[52:53], v[86:87], v[20:21] op_sel_hi:[1,0,1]
	v_add_f32_e32 v23, v10, v14
	s_waitcnt lgkmcnt(0)
	v_mov_b32_e32 v9, v54
	v_max_f32_e32 v10, 0, v7
	v_mov_b32_e32 v54, v17
	v_max_f32_e32 v14, 0, v22
	v_pk_fma_f32 v[8:9], v[8:9], v[10:11], v[20:21] op_sel_hi:[1,0,1]
	v_mov_b32_e32 v12, v18
	v_mov_b32_e32 v13, v56
	v_max_f32_e32 v16, 0, v23
	v_pk_fma_f32 v[8:9], v[54:55], v[14:15], v[8:9] op_sel_hi:[1,0,1]
	v_max_f32_e32 v22, 0, v11
	v_pk_fma_f32 v[8:9], v[12:13], v[16:17], v[8:9] op_sel_hi:[1,0,1]
	v_mov_b32_e32 v56, v19
	ds_read_b128 v[10:13], v32 offset:52432
	ds_read_b128 v[14:17], v32 offset:52688
	ds_read_b128 v[18:21], v32 offset:52944
	v_pk_fma_f32 v[22:23], v[56:57], v[22:23], v[8:9] op_sel_hi:[1,0,1]
	v_and_b32_e32 v24, 64, v84
	v_xor_b32_e32 v7, 16, v84
	v_add_u32_e32 v8, 64, v24
	v_cmp_lt_i32_e64 s[6:7], v7, v8
	s_and_b64 s[8:9], s[2:3], vcc
	s_waitcnt lgkmcnt(2)
	v_add_f32_e32 v9, v0, v10
	v_add_f32_e32 v11, v1, v11
	s_waitcnt lgkmcnt(1)
	v_mov_b32_e32 v0, v14
	s_waitcnt lgkmcnt(0)
	v_mov_b32_e32 v1, v18
	v_max_f32_e32 v10, 0, v9
	v_add_f32_e32 v24, v2, v12
	v_add_f32_e32 v13, v3, v13
	v_mov_b32_e32 v18, v15
	v_max_f32_e32 v12, 0, v11
	v_pk_fma_f32 v[0:1], v[0:1], v[10:11], v[22:23] op_sel_hi:[1,0,1]
	v_mov_b32_e32 v2, v16
	v_mov_b32_e32 v3, v20
	v_max_f32_e32 v14, 0, v24
	v_pk_fma_f32 v[0:1], v[18:19], v[12:13], v[0:1] op_sel_hi:[1,0,1]
	v_cndmask_b32_e64 v7, v84, v7, s[6:7]
	v_mov_b32_e32 v20, v17
	v_max_f32_e32 v16, 0, v13
	v_pk_fma_f32 v[0:1], v[2:3], v[14:15], v[0:1] op_sel_hi:[1,0,1]
	v_lshlrev_b32_e32 v7, 2, v7
	v_pk_fma_f32 v[0:1], v[20:21], v[16:17], v[0:1] op_sel_hi:[1,0,1]
	ds_bpermute_b32 v2, v7, v0
	ds_bpermute_b32 v3, v7, v1
	v_xor_b32_e32 v7, 32, v84
	v_cmp_lt_i32_e64 s[6:7], v7, v8
	v_mov_b32_e32 v10, -1
	s_waitcnt lgkmcnt(0)
	v_pk_add_f32 v[0:1], v[0:1], v[2:3]
	v_cndmask_b32_e64 v7, v84, v7, s[6:7]
	v_lshlrev_b32_e32 v7, 2, v7
	ds_bpermute_b32 v2, v7, v0
	ds_bpermute_b32 v3, v7, v1
	v_mov_b32_e32 v7, 0
	s_and_saveexec_b64 s[6:7], s[8:9]
	s_cbranch_execz .LBB5_108
	v_mov_b32_e32 v10, v103
	s_waitcnt lgkmcnt(0)
	v_pk_add_f32 v[4:5], v[0:1], v[2:3]
	v_mov_b32_e32 v7, 1.0
